# k_final epilogue: each thread reduces 4 consecutive d and issues two 16-byte write-through stores (was 8 dword stores)
# speedup vs baseline: 1.0131x; 1.0015x over previous
.LBB0_6:
	s_or_b64 exec, exec, s[4:5]
	s_waitcnt lgkmcnt(0)
	s_barrier
	ds_read_b32 v19, v29
	v_lshl_add_u32 v26, v26, s8, v27
	ds_read_b32 v27, v30
	ds_read_b32 v28, v28
	ds_read_b32 v25, v25
	s_waitcnt vmcnt(3)
	v_cmp_eq_u32_e32 vcc, 0, v17
	s_mov_b64 s[4:5], -1
	s_waitcnt lgkmcnt(3)
	v_add_lshl_u32 v19, v26, v19, 2
	ds_write2st64_b32 v19, v8, v9 offset1:64
	v_bfrev_b32_e32 v8, 1
	v_cndmask_b32_e32 v8, 0, v8, vcc
	v_or_b32_e32 v8, v8, v0
	ds_write_b32 v19, v8 offset:32768
	v_lshl_add_u32 v8, v20, s8, v21
	s_waitcnt lgkmcnt(4)
	v_add_lshl_u32 v8, v8, v27, 2
	ds_write2st64_b32 v8, v4, v5 offset1:64
	v_mov_b32_e32 v4, 0x400
	v_mov_b32_e32 v5, 0x80000400
	s_waitcnt vmcnt(2)
	v_cmp_eq_u32_e32 vcc, 0, v16
	s_nop 1
	v_cndmask_b32_e32 v4, v4, v5, vcc
	v_or_b32_e32 v4, v4, v0
	ds_write_b32 v8, v4 offset:32768
	v_lshl_add_u32 v4, v22, s8, v23
	s_waitcnt lgkmcnt(5)
	v_add_lshl_u32 v4, v4, v28, 2
	ds_write2st64_b32 v4, v6, v7 offset1:64
	v_mov_b32_e32 v5, 0x800
	v_mov_b32_e32 v6, 0x80000800
	s_waitcnt vmcnt(1)
	v_cmp_eq_u32_e32 vcc, 0, v15
	s_nop 1
	v_cndmask_b32_e32 v5, v5, v6, vcc
	v_or_b32_e32 v5, v5, v0
	ds_write_b32 v4, v5 offset:32768
	v_lshl_add_u32 v4, v24, s8, v18
	s_waitcnt lgkmcnt(6)
	v_add_lshl_u32 v4, v4, v25, 2
	ds_write2st64_b32 v4, v2, v3 offset1:64
	v_mov_b32_e32 v2, 0xc00
	v_mov_b32_e32 v3, 0x80000c00
	s_waitcnt vmcnt(0)
	v_cmp_eq_u32_e32 vcc, 0, v14
	s_nop 1
	v_cndmask_b32_e32 v2, v2, v3, vcc
	v_or_b32_e32 v2, v2, v0
	ds_write_b32 v4, v2 offset:32768
	s_waitcnt lgkmcnt(0)
	s_barrier
	s_getpc_b64 s[30:31]
	s_add_u32 s30, s30, 0x20b8
	s_addc_u32 s31, s31, 0
	v_lshlrev_b32_e32 v40, 6, v0
	v_min_u32_e32 v40, 0x2f00, v40
	global_load_dword v40, v40, s[30:31]
	s_and_b32 s32, s0, 0xfffff000
	s_mov_b32 s33, s1
	v_and_b32_e32 v41, 63, v0
	v_lshlrev_b32_e32 v41, 6, v41
	global_load_dword v41, v41, s[32:33]
	ds_read_b32 v14, v11 offset:32768
	s_mov_b64 s[18:19], s[44:45]
	s_mov_b64 s[8:9], s[36:37]
	s_mov_b64 s[10:11], s[38:39]
	s_mov_b64 s[12:13], s[40:41]
	s_mov_b64 s[14:15], s[42:43]
	ds_read2st64_b32 v[4:5], v11 offset1:64
	v_or_b32_e32 v2, s16, v0
	v_mov_b32_e32 v3, 0
	s_waitcnt lgkmcnt(0)
	v_and_b32_e32 v15, 0x7fffffff, v14
	s_and_b64 vcc, exec, s[2:3]
	v_lshlrev_b64 v[6:7], 2, v[2:3]
	s_cbranch_vccz .LBB0_8
	v_lshl_add_u64 v[8:9], s[10:11], 0, v[6:7]
	global_store_dword v[8:9], v4, off
	v_lshl_add_u64 v[8:9], s[12:13], 0, v[6:7]
	global_store_dword v[8:9], v5, off
	v_lshl_add_u64 v[8:9], s[14:15], 0, v[6:7]
	global_store_dword v[8:9], v15, off
	s_mov_b64 s[4:5], 0

.LBB1_37:
	v_lshrrev_b32_e32 v18, 5, v1
	s_mulk_i32 s20, 0x4100
	v_mul_u32_u24_e32 v18, 0x410, v18
	v_lshlrev_b32_e32 v19, 2, v143
	v_add3_u32 v18, s20, v18, v19
	v_add_u32_e32 v19, 0x800, v18
	s_nop 0
	ds_write2_b32 v18, v50, v66 offset1:32
	ds_write2_b32 v18, v51, v67 offset0:65 offset1:97
	ds_write2_b32 v18, v52, v68 offset0:130 offset1:162
	ds_write2_b32 v18, v53, v69 offset0:195 offset1:227
	ds_write2_b32 v19, v54, v70 offset0:8 offset1:40
	ds_write2_b32 v19, v55, v71 offset0:73 offset1:105
	ds_write2_b32 v19, v56, v72 offset0:138 offset1:170
	ds_write2_b32 v19, v57, v73 offset0:203 offset1:235
	v_add_u32_e32 v19, 0x1000, v18
	ds_write2_b32 v19, v58, v74 offset0:16 offset1:48
	ds_write2_b32 v19, v59, v75 offset0:81 offset1:113
	ds_write2_b32 v19, v60, v76 offset0:146 offset1:178
	ds_write2_b32 v19, v61, v77 offset0:211 offset1:243
	v_add_u32_e32 v19, 0x1800, v18
	ds_write2_b32 v19, v62, v78 offset0:24 offset1:56
	ds_write2_b32 v19, v63, v79 offset0:89 offset1:121
	ds_write2_b32 v19, v64, v80 offset0:154 offset1:186
	ds_write2_b32 v19, v65, v81 offset0:219 offset1:251
	v_add_u32_e32 v19, 0x2000, v18
	ds_write2_b32 v19, v34, v2 offset0:32 offset1:64
	ds_write2_b32 v19, v35, v3 offset0:97 offset1:129
	ds_write2_b32 v19, v36, v4 offset0:162 offset1:194
	v_add_u32_e32 v2, 0x2200, v18
	ds_write2_b32 v2, v37, v5 offset0:99 offset1:131
	v_add_u32_e32 v2, 0x2800, v18
	ds_write2_b32 v2, v38, v6 offset0:40 offset1:72
	ds_write2_b32 v2, v39, v7 offset0:105 offset1:137
	ds_write2_b32 v2, v40, v8 offset0:170 offset1:202
	v_add_u32_e32 v2, 0x2a00, v18
	ds_write2_b32 v2, v41, v9 offset0:107 offset1:139
	v_add_u32_e32 v2, 0x3000, v18
	ds_write2_b32 v2, v42, v10 offset0:48 offset1:80
	ds_write2_b32 v2, v43, v11 offset0:113 offset1:145
	ds_write2_b32 v2, v44, v12 offset0:178 offset1:210
	v_add_u32_e32 v2, 0x3200, v18
	v_lshrrev_b32_e32 v4, 4, v0
	ds_write2_b32 v2, v45, v13 offset0:115 offset1:147
	v_add_u32_e32 v2, 0x3800, v18
	s_waitcnt vmcnt(3)
	v_and_b32_e32 v20, 28, v4
	s_movk_i32 s0, 0x104
	ds_write2_b32 v2, v46, v14 offset0:56 offset1:88
	ds_write2_b32 v2, v47, v15 offset0:121 offset1:153
	ds_write2_b32 v2, v48, v16 offset0:186 offset1:218
	v_add_u32_e32 v2, 0x3a00, v18
	v_mad_u32_u24 v21, v1, s0, v20
	ds_write2_b32 v2, v49, v17 offset0:123 offset1:155
	s_waitcnt lgkmcnt(0)
	s_barrier
	v_and_b32_e32 v2, 15, v0
	v_lshrrev_b32_e32 v3, 4, v0
	v_mul_u32_u24_e32 v4, 0x104, v2
	v_add_lshl_u32 v4, v4, v3, 2
	v_add_u32_e32 v5, 0x10400, v4
	v_mov_b32_e32 v6, 0x23800
	v_lshl_add_u32 v6, v3, 2, v6
	ds_read2_b32 v[8:9], v6 offset1:64
	ds_read2_b32 v[10:11], v6 offset0:32 offset1:96
	s_waitcnt lgkmcnt(0)
	ds_read_b32 v12, v4 offset:0
	ds_read_b32 v13, v4 offset:16640
	ds_read_b32 v14, v4 offset:33280
	ds_read_b32 v15, v4 offset:49920
	ds_read_b32 v16, v5 offset:0
	ds_read_b32 v17, v5 offset:16640
	ds_read_b32 v18, v5 offset:33280
	ds_read_b32 v19, v5 offset:49920
	ds_read_b32 v20, v4 offset:260
	ds_read_b32 v21, v4 offset:16900
	ds_read_b32 v22, v4 offset:33540
	ds_read_b32 v23, v4 offset:50180
	s_waitcnt lgkmcnt(8)
	v_add_f32_e32 v12, v12, v13
	v_add_f32_e32 v14, v14, v15
	v_add_f32_e32 v24, v12, v14
	ds_read_b32 v12, v5 offset:260
	ds_read_b32 v13, v5 offset:16900
	ds_read_b32 v14, v5 offset:33540
	ds_read_b32 v15, v5 offset:50180
	s_waitcnt lgkmcnt(8)
	v_add_f32_e32 v16, v16, v17
	v_add_f32_e32 v18, v18, v19
	v_add_f32_e32 v16, v16, v18
	v_add_f32_e32 v24, v24, v16
	ds_read_b32 v16, v4 offset:520
	ds_read_b32 v17, v4 offset:17160
	ds_read_b32 v18, v4 offset:33800
	ds_read_b32 v19, v4 offset:50440
	s_waitcnt lgkmcnt(8)
	v_add_f32_e32 v20, v20, v21
	v_add_f32_e32 v22, v22, v23
	v_add_f32_e32 v25, v20, v22
	ds_read_b32 v20, v5 offset:520
	ds_read_b32 v21, v5 offset:17160
	ds_read_b32 v22, v5 offset:33800
	ds_read_b32 v23, v5 offset:50440
	s_waitcnt lgkmcnt(8)
	v_add_f32_e32 v12, v12, v13
	v_add_f32_e32 v14, v14, v15
	v_add_f32_e32 v12, v12, v14
	v_add_f32_e32 v25, v25, v12
	ds_read_b32 v12, v4 offset:780
	ds_read_b32 v13, v4 offset:17420
	ds_read_b32 v14, v4 offset:34060
	ds_read_b32 v15, v4 offset:50700
	s_waitcnt lgkmcnt(8)
	v_add_f32_e32 v16, v16, v17
	v_add_f32_e32 v18, v18, v19
	v_add_f32_e32 v26, v16, v18
	ds_read_b32 v16, v5 offset:780
	ds_read_b32 v17, v5 offset:17420
	ds_read_b32 v18, v5 offset:34060
	ds_read_b32 v19, v5 offset:50700
	s_waitcnt lgkmcnt(8)
	v_add_f32_e32 v20, v20, v21
	v_add_f32_e32 v22, v22, v23
	v_add_f32_e32 v20, v20, v22
	v_add_f32_e32 v26, v26, v20
	ds_read_b32 v20, v4 offset:128
	ds_read_b32 v21, v4 offset:16768
	ds_read_b32 v22, v4 offset:33408
	ds_read_b32 v23, v4 offset:50048
	s_waitcnt lgkmcnt(8)
	v_add_f32_e32 v12, v12, v13
	v_add_f32_e32 v14, v14, v15
	v_add_f32_e32 v27, v12, v14
	ds_read_b32 v12, v5 offset:128
	ds_read_b32 v13, v5 offset:16768
	ds_read_b32 v14, v5 offset:33408
	ds_read_b32 v15, v5 offset:50048
	s_waitcnt lgkmcnt(8)
	v_add_f32_e32 v16, v16, v17
	v_add_f32_e32 v18, v18, v19
	v_add_f32_e32 v16, v16, v18
	v_add_f32_e32 v27, v27, v16
	ds_read_b32 v16, v4 offset:388
	ds_read_b32 v17, v4 offset:17028
	ds_read_b32 v18, v4 offset:33668
	ds_read_b32 v19, v4 offset:50308
	s_waitcnt lgkmcnt(8)
	v_add_f32_e32 v20, v20, v21
	v_add_f32_e32 v22, v22, v23
	v_add_f32_e32 v28, v20, v22
	ds_read_b32 v20, v5 offset:388
	ds_read_b32 v21, v5 offset:17028
	ds_read_b32 v22, v5 offset:33668
	ds_read_b32 v23, v5 offset:50308
	s_waitcnt lgkmcnt(8)
	v_add_f32_e32 v12, v12, v13
	v_add_f32_e32 v14, v14, v15
	v_add_f32_e32 v12, v12, v14
	v_add_f32_e32 v28, v28, v12
	ds_read_b32 v12, v4 offset:648
	ds_read_b32 v13, v4 offset:17288
	ds_read_b32 v14, v4 offset:33928
	ds_read_b32 v15, v4 offset:50568
	s_waitcnt lgkmcnt(8)
	v_add_f32_e32 v16, v16, v17
	v_add_f32_e32 v18, v18, v19
	v_add_f32_e32 v29, v16, v18
	ds_read_b32 v16, v5 offset:648
	ds_read_b32 v17, v5 offset:17288
	ds_read_b32 v18, v5 offset:33928
	ds_read_b32 v19, v5 offset:50568
	s_waitcnt lgkmcnt(8)
	v_add_f32_e32 v20, v20, v21
	v_add_f32_e32 v22, v22, v23
	v_add_f32_e32 v20, v20, v22
	v_add_f32_e32 v29, v29, v20
	ds_read_b32 v20, v4 offset:908
	ds_read_b32 v21, v4 offset:17548
	ds_read_b32 v22, v4 offset:34188
	ds_read_b32 v23, v4 offset:50828
	s_waitcnt lgkmcnt(8)
	v_add_f32_e32 v12, v12, v13
	v_add_f32_e32 v14, v14, v15
	v_add_f32_e32 v30, v12, v14
	ds_read_b32 v12, v5 offset:908
	ds_read_b32 v13, v5 offset:17548
	ds_read_b32 v14, v5 offset:34188
	ds_read_b32 v15, v5 offset:50828
	s_waitcnt lgkmcnt(8)
	v_add_f32_e32 v16, v16, v17
	v_add_f32_e32 v18, v18, v19
	v_add_f32_e32 v16, v16, v18
	v_add_f32_e32 v30, v30, v16
	s_waitcnt lgkmcnt(4)
	v_add_f32_e32 v20, v20, v21
	v_add_f32_e32 v22, v22, v23
	v_add_f32_e32 v31, v20, v22
	s_waitcnt lgkmcnt(0)
	v_add_f32_e32 v12, v12, v13
	v_add_f32_e32 v14, v14, v15
	v_add_f32_e32 v12, v12, v14
	v_add_f32_e32 v31, v31, v12
	v_mul_f32_e32 v24, v24, v9
	v_mul_f32_e32 v25, v25, v9
	v_mul_f32_e32 v26, v26, v9
	v_mul_f32_e32 v27, v27, v9
	v_mul_f32_e32 v28, v28, v11
	v_mul_f32_e32 v29, v29, v11
	v_mul_f32_e32 v30, v30, v11
	v_mul_f32_e32 v31, v31, v11
	v_add_lshl_u32 v32, v8, s8, 8
	v_add_lshl_u32 v33, v10, s8, 8
	v_lshl_add_u32 v32, v2, 4, v32
	v_lshl_add_u32 v33, v2, 4, v33
	global_store_dwordx4 v32, v[24:27], s[10:11] sc1
	global_store_dwordx4 v33, v[28:31], s[10:11] sc1
	s_endpgm

.LBB4_39:
	s_waitcnt vmcnt(5)
	v_rcp_f32_e32 v2, v133
	s_waitcnt vmcnt(4)
	v_rcp_f32_e32 v3, v132
	s_waitcnt vmcnt(3)
	v_rcp_f32_e32 v4, v131
	v_cmp_lt_f32_e32 vcc, 0, v133
	s_waitcnt vmcnt(2)
	v_rcp_f32_e32 v5, v130
	s_waitcnt vmcnt(1)
	v_rcp_f32_e32 v6, v129
	v_cndmask_b32_e32 v2, 0, v2, vcc
	v_cmp_lt_f32_e32 vcc, 0, v132
	s_waitcnt vmcnt(0)
	v_rcp_f32_e32 v7, v128
	s_getpc_b64 s[36:37]
	s_sub_u32 s36, s36, 0x9238
	s_subb_u32 s37, s37, 0
	v_lshlrev_b32_e32 v183, 6, v0
	v_min_u32_e32 v183, 0x1d80, v183
	global_load_dword v183, v183, s[36:37]
	v_lshlrev_b32_e32 v182, 6, v38
	global_load_dword v182, v182, s[38:39]
	s_lshl_b32 s40, s29, 10
	s_add_u32 s40, s42, s40
	s_addc_u32 s41, s43, 0
	v_lshlrev_b32_e32 v181, 6, v0
	v_and_b32_e32 v181, 0x7fc0, v181
	global_load_dword v181, v181, s[40:41]
	s_mov_b32 s4, 0x42c80000
	v_cndmask_b32_e32 v3, 0, v3, vcc
	v_cmp_lt_f32_e32 vcc, 0, v131
	v_cmp_ngt_f32_e64 s[2:3], s4, v3
	s_mov_b64 s[6:7], 0
	v_cndmask_b32_e32 v4, 0, v4, vcc
	v_cmp_lt_f32_e32 vcc, 0, v130
	s_nop 1
	v_cndmask_b32_e32 v5, 0, v5, vcc
	v_cmp_lt_f32_e32 vcc, 0, v129
	s_nop 1
	v_cndmask_b32_e32 v6, 0, v6, vcc
	v_cmp_lt_f32_e32 vcc, 0, v128
	s_nop 1
	v_cndmask_b32_e32 v7, 0, v7, vcc
	v_cmp_ngt_f32_e32 vcc, s4, v2
	s_or_b64 s[2:3], vcc, s[2:3]
	v_cmp_ngt_f32_e32 vcc, s4, v4
	s_or_b64 s[2:3], s[2:3], vcc
	v_cmp_ngt_f32_e32 vcc, s4, v5
	s_or_b64 s[2:3], s[2:3], vcc
	v_cmp_ngt_f32_e32 vcc, s4, v6
	s_or_b64 s[2:3], s[2:3], vcc
	v_cmp_ngt_f32_e32 vcc, s4, v7
	s_or_b64 s[2:3], s[2:3], vcc
	v_cndmask_b32_e64 v8, 0, 1, s[2:3]
	v_cmp_ne_u32_e32 vcc, 0, v8
	s_cmp_eq_u64 vcc, 0
	s_cselect_b64 s[2:3], -1, 0
	v_cndmask_b32_e64 v8, 0, 1, s[2:3]
	s_nop 0
	v_readfirstlane_b32 s2, v8
	s_bitcmp0_b32 s2, 0
	s_cbranch_scc0 .LBB4_45
	s_cmp_lt_i32 s28, 4
	s_cbranch_scc1 .LBB4_46
	s_cmp_gt_i32 s28, 4
	s_cbranch_scc0 .LBB4_47
	s_mov_b64 s[4:5], -1
	v_mov_b32_e32 v8, 0
	s_cmp_gt_i32 s28, 5
	v_mov_b32_e32 v167, 0
	v_mov_b32_e32 v166, 0
	v_mov_b32_e32 v165, 0
	v_mov_b32_e32 v164, 0
	v_mov_b32_e32 v162, 0
	v_mov_b32_e32 v160, 0
	v_mov_b32_e32 v159, 0
	v_mov_b32_e32 v157, 0
	v_mov_b32_e32 v151, 0
	v_mov_b32_e32 v149, 0
	v_mov_b32_e32 v147, 0
	v_mov_b32_e32 v146, 0
	v_mov_b32_e32 v144, 0
	v_mov_b32_e32 v143, 0
	v_mov_b32_e32 v152, 0
	v_mov_b32_e32 v153, 0
	v_mov_b32_e32 v154, 0
	v_mov_b32_e32 v155, 0
	v_mov_b32_e32 v156, 0
	v_mov_b32_e32 v158, 0
	v_mov_b32_e32 v161, 0
	v_mov_b32_e32 v163, 0
	v_mov_b32_e32 v168, 0
	v_mov_b32_e32 v169, 0
	v_mov_b32_e32 v170, 0
	v_mov_b32_e32 v171, 0
	v_mov_b32_e32 v172, 0
	v_mov_b32_e32 v173, 0
	v_mov_b32_e32 v174, 0
	v_mov_b32_e32 v145, 0
	v_mov_b32_e32 v148, 0
	v_mov_b32_e32 v150, 0
	s_cbranch_scc0 .LBB4_50
	s_cmp_eq_u32 s28, 6
	s_cbranch_scc0 .LBB4_49
	v_mov_b32_e32 v145, 0
	v_mov_b32_e32 v148, 0
	v_mov_b32_e32 v150, 0
	v_mov_b32_e32 v143, 0
	v_mov_b32_e32 v144, 0
	v_mov_b32_e32 v146, 0
	v_mov_b32_e32 v147, 0
	v_mov_b32_e32 v149, 0
	v_mov_b32_e32 v151, 0
	v_mov_b32_e32 v152, 0
	v_mov_b32_e32 v153, 0
	v_mov_b32_e32 v154, 0
	v_mov_b32_e32 v155, 0
	v_mov_b32_e32 v156, 0
	v_mov_b32_e32 v158, 0
	v_mov_b32_e32 v161, 0
	v_mov_b32_e32 v163, 0
	v_mov_b32_e32 v157, 0
	v_mov_b32_e32 v159, 0
	v_mov_b32_e32 v160, 0
	v_mov_b32_e32 v162, 0
	v_mov_b32_e32 v164, 0
	v_mov_b32_e32 v165, 0
	v_mov_b32_e32 v166, 0
	v_mov_b32_e32 v167, 0
	v_mov_b32_e32 v168, 0
	v_mov_b32_e32 v169, 0
	v_mov_b32_e32 v170, 0
	v_mov_b32_e32 v171, 0
	v_mov_b32_e32 v172, 0
	v_mov_b32_e32 v173, 0
	v_mov_b32_e32 v174, 0
	v_fma_mix_f32 v148, v43, v7, v148 op_sel_hi:[1,0,0]
	v_fma_mix_f32 v150, v45, v7, v150 op_sel_hi:[1,0,0]
	v_fma_mix_f32 v143, v50, v7, v143 op_sel_hi:[1,0,0]
	v_fma_mix_f32 v144, v54, v7, v144 op_sel_hi:[1,0,0]
	v_fma_mix_f32 v146, v58, v7, v146 op_sel_hi:[1,0,0]
	v_fma_mix_f32 v147, v61, v7, v147 op_sel_hi:[1,0,0]
	v_fma_mix_f32 v149, v64, v7, v149 op_sel_hi:[1,0,0]
	v_fma_mix_f32 v151, v66, v7, v151 op_sel_hi:[1,0,0]
	v_fma_mix_f32 v152, v43, v7, v152 op_sel:[1,0,0] op_sel_hi:[1,0,0]
	v_fma_mix_f32 v153, v45, v7, v153 op_sel:[1,0,0] op_sel_hi:[1,0,0]
	v_fma_mix_f32 v154, v50, v7, v154 op_sel:[1,0,0] op_sel_hi:[1,0,0]
	v_fma_mix_f32 v155, v54, v7, v155 op_sel:[1,0,0] op_sel_hi:[1,0,0]
	v_fma_mix_f32 v156, v58, v7, v156 op_sel:[1,0,0] op_sel_hi:[1,0,0]
	v_fma_mix_f32 v158, v61, v7, v158 op_sel:[1,0,0] op_sel_hi:[1,0,0]
	v_fma_mix_f32 v161, v64, v7, v161 op_sel:[1,0,0] op_sel_hi:[1,0,0]
	v_fma_mix_f32 v163, v66, v7, v163 op_sel:[1,0,0] op_sel_hi:[1,0,0]
	v_fma_mix_f32 v157, v72, v7, v157 op_sel_hi:[1,0,0]
	v_fma_mix_f32 v159, v76, v7, v159 op_sel_hi:[1,0,0]
	v_fma_mix_f32 v160, v83, v7, v160 op_sel_hi:[1,0,0]
	v_fma_mix_f32 v162, v85, v7, v162 op_sel_hi:[1,0,0]
	v_fma_mix_f32 v164, v89, v7, v164 op_sel_hi:[1,0,0]
	v_fma_mix_f32 v165, v92, v7, v165 op_sel_hi:[1,0,0]
	v_fma_mix_f32 v166, v95, v7, v166 op_sel_hi:[1,0,0]
	v_fma_mix_f32 v167, v96, v7, v167 op_sel_hi:[1,0,0]
	v_fma_mix_f32 v168, v72, v7, v168 op_sel:[1,0,0] op_sel_hi:[1,0,0]
	v_fma_mix_f32 v169, v76, v7, v169 op_sel:[1,0,0] op_sel_hi:[1,0,0]
	v_fma_mix_f32 v170, v83, v7, v170 op_sel:[1,0,0] op_sel_hi:[1,0,0]
	v_fma_mix_f32 v171, v85, v7, v171 op_sel:[1,0,0] op_sel_hi:[1,0,0]
	v_fma_mix_f32 v172, v89, v7, v172 op_sel:[1,0,0] op_sel_hi:[1,0,0]
	v_fma_mix_f32 v173, v92, v7, v173 op_sel:[1,0,0] op_sel_hi:[1,0,0]
	v_fma_mix_f32 v174, v95, v7, v174 op_sel:[1,0,0] op_sel_hi:[1,0,0]
	v_fma_mix_f32 v145, v96, v7, v145 op_sel:[1,0,0] op_sel_hi:[1,0,0]
	s_branch .LBB4_50
